# dense SwiGLU-up GEMM: L2 prefetch one K-tile ahead of the staging loads (one dword LDS-DMA load per wave and K-tile into a scratch LDS slot)
# baseline (speedup 1.0000x reference)
.LBB0_574:
	ds_read_b128 v[146:149], v152
	ds_read_b128 v[156:159], v152 offset:1024
	ds_read_b128 v[160:163], v152 offset:2048
	ds_read_b128 v[164:167], v152 offset:3072
	ds_read_b128 v[168:171], v153
	ds_read_b128 v[172:175], v153 offset:1024
	ds_read_b128 v[176:179], v153 offset:2048
	ds_read_b128 v[180:183], v153 offset:3072
	s_add_u32 s24, s22, 0xfff80080
	s_addc_u32 s25, s23, -1
	s_cmp_eq_u32 s69, 28
	s_cselect_b32 s27, s15, s25
	s_cselect_b32 s26, s65, s24
	s_cselect_b32 s25, s13, s68
	s_cselect_b32 s24, s66, s67
	v_lshl_add_u64 v[216:217], s[22:23], 0, v[138:139]
	s_add_i32 m0, s21, 0xc000
	ds_read_b128 v[184:187], v154
	ds_read_b128 v[188:191], v154 offset:1024
	ds_read_b128 v[192:195], v154 offset:2048
	ds_read_b128 v[196:199], v154 offset:3072
	ds_read_b128 v[200:203], v154 offset:4096
	ds_read_b128 v[204:207], v154 offset:5120
	ds_read_b128 v[208:211], v154 offset:6144
	ds_read_b128 v[212:215], v154 offset:7168
	global_load_lds_dwordx4 v[216:217], off
	v_lshl_add_u64 v[216:217], s[22:23], 0, v[140:141]
	s_add_i32 m0, s21, 0xe000
	s_nop 0
	global_load_lds_dwordx4 v[216:217], off
	s_waitcnt vmcnt(9)
	s_waitcnt lgkmcnt(0)
	s_barrier
	s_setprio 1
	s_waitcnt lgkmcnt(0)
	v_mfma_f32_16x16x32_bf16 v[126:129], v[146:149], v[184:187], v[126:129]
	v_mfma_f32_16x16x32_bf16 v[122:125], v[160:163], v[184:187], v[122:125]
	v_mfma_f32_16x16x32_bf16 v[110:113], v[146:149], v[192:195], v[110:113]
	v_mfma_f32_16x16x32_bf16 v[106:109], v[160:163], v[192:195], v[106:109]
	v_mfma_f32_16x16x32_bf16 v[94:97], v[146:149], v[200:203], v[94:97]
	v_mfma_f32_16x16x32_bf16 v[90:93], v[160:163], v[200:203], v[90:93]
	v_mfma_f32_16x16x32_bf16 v[78:81], v[146:149], v[208:211], v[78:81]
	v_mfma_f32_16x16x32_bf16 v[74:77], v[160:163], v[208:211], v[74:77]
	v_mfma_f32_16x16x32_bf16 v[126:129], v[156:159], v[188:191], v[126:129]
	v_mfma_f32_16x16x32_bf16 v[122:125], v[164:167], v[188:191], v[122:125]
	v_mfma_f32_16x16x32_bf16 v[110:113], v[156:159], v[196:199], v[110:113]
	v_mfma_f32_16x16x32_bf16 v[106:109], v[164:167], v[196:199], v[106:109]
	v_mfma_f32_16x16x32_bf16 v[94:97], v[156:159], v[204:207], v[94:97]
	v_mfma_f32_16x16x32_bf16 v[90:93], v[164:167], v[204:207], v[90:93]
	v_mfma_f32_16x16x32_bf16 v[78:81], v[156:159], v[212:215], v[78:81]
	v_mfma_f32_16x16x32_bf16 v[74:77], v[164:167], v[212:215], v[74:77]
	s_setprio 0
	s_setprio 1
	v_mfma_f32_16x16x32_bf16 v[118:121], v[168:171], v[184:187], v[118:121]
	v_mfma_f32_16x16x32_bf16 v[114:117], v[176:179], v[184:187], v[114:117]
	v_mfma_f32_16x16x32_bf16 v[102:105], v[168:171], v[192:195], v[102:105]
	v_mfma_f32_16x16x32_bf16 v[98:101], v[176:179], v[192:195], v[98:101]
	v_mfma_f32_16x16x32_bf16 v[86:89], v[168:171], v[200:203], v[86:89]
	v_mfma_f32_16x16x32_bf16 v[82:85], v[176:179], v[200:203], v[82:85]
	v_mfma_f32_16x16x32_bf16 v[70:73], v[168:171], v[208:211], v[70:73]
	v_mfma_f32_16x16x32_bf16 v[66:69], v[176:179], v[208:211], v[66:69]
	v_mfma_f32_16x16x32_bf16 v[118:121], v[172:175], v[188:191], v[118:121]
	v_mfma_f32_16x16x32_bf16 v[114:117], v[180:183], v[188:191], v[114:117]
	v_mfma_f32_16x16x32_bf16 v[102:105], v[172:175], v[196:199], v[102:105]
	v_mfma_f32_16x16x32_bf16 v[98:101], v[180:183], v[196:199], v[98:101]
	v_mfma_f32_16x16x32_bf16 v[86:89], v[172:175], v[204:207], v[86:89]
	v_mfma_f32_16x16x32_bf16 v[82:85], v[180:183], v[204:207], v[82:85]
	v_mfma_f32_16x16x32_bf16 v[70:73], v[172:175], v[212:215], v[70:73]
	v_mfma_f32_16x16x32_bf16 v[66:69], v[180:183], v[212:215], v[66:69]
	s_setprio 0
	s_barrier
	s_add_i32 s70, s61, s33
	v_lshl_add_u64 v[216:217], s[24:25], 0, v[134:135]
	s_mov_b32 m0, s70
	ds_read_b128 v[184:187], v154 offset:16384
	ds_read_b128 v[188:191], v154 offset:17408
	ds_read_b128 v[192:195], v154 offset:18432
	ds_read_b128 v[196:199], v154 offset:19456
	ds_read_b128 v[200:203], v154 offset:20480
	ds_read_b128 v[204:207], v154 offset:21504
	ds_read_b128 v[208:211], v154 offset:22528
	ds_read_b128 v[212:215], v154 offset:23552
	global_load_lds_dwordx4 v[216:217], off
	s_add_i32 m0, s70, 0x2000
	s_add_u32 s70, s24, 0x80000
	v_lshl_add_u64 v[218:219], s[24:25], 0, v[130:131]
	s_addc_u32 s71, s25, 0
	s_add_i32 s72, s62, s33
	global_load_lds_dwordx4 v[218:219], off
	v_lshl_add_u64 v[220:221], s[70:71], 0, v[134:135]
	s_mov_b32 m0, s72
	v_lshl_add_u64 v[222:223], s[26:27], 0, v[132:133]
	global_load_lds_dwordx4 v[220:221], off
	v_lshl_add_u64 v[220:221], s[70:71], 0, v[130:131]
	s_add_i32 m0, s72, 0x2000
	s_nop 0
	global_load_lds_dwordx4 v[220:221], off
	v_lshl_add_u64 v[220:221], s[26:27], 0, v[136:137]
	s_mov_b32 m0, s21
	s_nop 0
	global_load_lds_dwordx4 v[220:221], off
	s_mov_b32 m0, s36
	s_nop 0
	global_load_lds_dwordx4 v[222:223], off
	s_cmp_lg_u32 s100, 0
	s_cselect_b32 s98, s24, s26
	s_cselect_b32 s99, s25, s27
	s_add_u32 s98, s98, 0x80
	s_addc_u32 s99, s99, 0
	s_mov_b32 m0, 0x21700
	s_nop 0
	global_load_lds_dword v252, s[98:99]
	s_waitcnt vmcnt(10)
	s_waitcnt lgkmcnt(0)
	s_barrier
	s_setprio 1
	s_waitcnt lgkmcnt(0)
	v_mfma_f32_16x16x32_bf16 v[62:65], v[146:149], v[184:187], v[62:65]
	v_mfma_f32_16x16x32_bf16 v[58:61], v[160:163], v[184:187], v[58:61]
	v_mfma_f32_16x16x32_bf16 v[46:49], v[146:149], v[192:195], v[46:49]
	v_mfma_f32_16x16x32_bf16 v[42:45], v[160:163], v[192:195], v[42:45]
	v_mfma_f32_16x16x32_bf16 v[30:33], v[146:149], v[200:203], v[30:33]
	v_mfma_f32_16x16x32_bf16 v[26:29], v[160:163], v[200:203], v[26:29]
	v_mfma_f32_16x16x32_bf16 v[14:17], v[146:149], v[208:211], v[14:17]
	v_mfma_f32_16x16x32_bf16 v[10:13], v[160:163], v[208:211], v[10:13]
	v_mfma_f32_16x16x32_bf16 v[62:65], v[156:159], v[188:191], v[62:65]
	v_mfma_f32_16x16x32_bf16 v[58:61], v[164:167], v[188:191], v[58:61]
	v_mfma_f32_16x16x32_bf16 v[46:49], v[156:159], v[196:199], v[46:49]
	v_mfma_f32_16x16x32_bf16 v[42:45], v[164:167], v[196:199], v[42:45]
	v_mfma_f32_16x16x32_bf16 v[30:33], v[156:159], v[204:207], v[30:33]
	v_mfma_f32_16x16x32_bf16 v[26:29], v[164:167], v[204:207], v[26:29]
	v_mfma_f32_16x16x32_bf16 v[14:17], v[156:159], v[212:215], v[14:17]
	v_mfma_f32_16x16x32_bf16 v[10:13], v[164:167], v[212:215], v[10:13]
	s_setprio 0
	s_setprio 1
	v_mfma_f32_16x16x32_bf16 v[54:57], v[168:171], v[184:187], v[54:57]
	v_mfma_f32_16x16x32_bf16 v[50:53], v[176:179], v[184:187], v[50:53]
	v_mfma_f32_16x16x32_bf16 v[38:41], v[168:171], v[192:195], v[38:41]
	v_mfma_f32_16x16x32_bf16 v[34:37], v[176:179], v[192:195], v[34:37]
	v_mfma_f32_16x16x32_bf16 v[22:25], v[168:171], v[200:203], v[22:25]
	v_mfma_f32_16x16x32_bf16 v[18:21], v[176:179], v[200:203], v[18:21]
	v_mfma_f32_16x16x32_bf16 v[6:9], v[168:171], v[208:211], v[6:9]
	v_mfma_f32_16x16x32_bf16 v[2:5], v[176:179], v[208:211], v[2:5]
	v_mfma_f32_16x16x32_bf16 v[54:57], v[172:175], v[188:191], v[54:57]
	v_mfma_f32_16x16x32_bf16 v[50:53], v[180:183], v[188:191], v[50:53]
	v_mfma_f32_16x16x32_bf16 v[38:41], v[172:175], v[196:199], v[38:41]
	v_mfma_f32_16x16x32_bf16 v[34:37], v[180:183], v[196:199], v[34:37]
	v_mfma_f32_16x16x32_bf16 v[22:25], v[172:175], v[204:207], v[22:25]
	v_mfma_f32_16x16x32_bf16 v[18:21], v[180:183], v[204:207], v[18:21]
	v_mfma_f32_16x16x32_bf16 v[6:9], v[172:175], v[212:215], v[6:9]
	v_mfma_f32_16x16x32_bf16 v[2:5], v[180:183], v[212:215], v[2:5]
	s_setprio 0
	s_barrier
	s_add_i32 s70, 0, 0x18000
	v_add_u32_e32 v155, s70, v150
	s_add_i32 s71, 0, 0x1c000
	ds_read_b128 v[146:149], v155
	ds_read_b128 v[156:159], v155 offset:1024
	ds_read_b128 v[160:163], v155 offset:2048
	ds_read_b128 v[164:167], v155 offset:3072
	v_add_u32_e32 v155, s71, v150
	ds_read_b128 v[168:171], v155
	ds_read_b128 v[172:175], v155 offset:1024
	ds_read_b128 v[176:179], v155 offset:2048
	ds_read_b128 v[180:183], v155 offset:3072
	s_add_u32 s26, s26, 0x80000
	s_addc_u32 s27, s27, 0
	s_mov_b32 m0, s37
	v_lshl_add_u64 v[224:225], s[26:27], 0, v[136:137]
	ds_read_b128 v[184:187], v154 offset:32768
	ds_read_b128 v[188:191], v154 offset:33792
	ds_read_b128 v[192:195], v154 offset:34816
	ds_read_b128 v[196:199], v154 offset:35840
	ds_read_b128 v[200:203], v154 offset:36864
	ds_read_b128 v[204:207], v154 offset:37888
	ds_read_b128 v[208:211], v154 offset:38912
	ds_read_b128 v[212:215], v154 offset:39936
	global_load_lds_dwordx4 v[224:225], off
	v_lshl_add_u64 v[224:225], s[26:27], 0, v[132:133]
	s_mov_b32 m0, s42
	s_nop 0
	global_load_lds_dwordx4 v[224:225], off
	s_waitcnt vmcnt(9)
	s_waitcnt lgkmcnt(0)
	s_barrier
	s_setprio 1
	s_waitcnt lgkmcnt(0)
	v_mfma_f32_16x16x32_bf16 v[126:129], v[146:149], v[184:187], v[126:129]
	v_mfma_f32_16x16x32_bf16 v[122:125], v[160:163], v[184:187], v[122:125]
	v_mfma_f32_16x16x32_bf16 v[110:113], v[146:149], v[192:195], v[110:113]
	v_mfma_f32_16x16x32_bf16 v[106:109], v[160:163], v[192:195], v[106:109]
	v_mfma_f32_16x16x32_bf16 v[94:97], v[146:149], v[200:203], v[94:97]
	v_mfma_f32_16x16x32_bf16 v[90:93], v[160:163], v[200:203], v[90:93]
	v_mfma_f32_16x16x32_bf16 v[78:81], v[146:149], v[208:211], v[78:81]
	v_mfma_f32_16x16x32_bf16 v[74:77], v[160:163], v[208:211], v[74:77]
	v_mfma_f32_16x16x32_bf16 v[126:129], v[156:159], v[188:191], v[126:129]
	v_mfma_f32_16x16x32_bf16 v[122:125], v[164:167], v[188:191], v[122:125]
	v_mfma_f32_16x16x32_bf16 v[110:113], v[156:159], v[196:199], v[110:113]
	v_mfma_f32_16x16x32_bf16 v[106:109], v[164:167], v[196:199], v[106:109]
	v_mfma_f32_16x16x32_bf16 v[94:97], v[156:159], v[204:207], v[94:97]
	v_mfma_f32_16x16x32_bf16 v[90:93], v[164:167], v[204:207], v[90:93]
	v_mfma_f32_16x16x32_bf16 v[78:81], v[156:159], v[212:215], v[78:81]
	v_mfma_f32_16x16x32_bf16 v[74:77], v[164:167], v[212:215], v[74:77]
	s_setprio 0
	s_setprio 1
	v_mfma_f32_16x16x32_bf16 v[118:121], v[168:171], v[184:187], v[118:121]
	v_mfma_f32_16x16x32_bf16 v[114:117], v[176:179], v[184:187], v[114:117]
	v_mfma_f32_16x16x32_bf16 v[102:105], v[168:171], v[192:195], v[102:105]
	v_mfma_f32_16x16x32_bf16 v[98:101], v[176:179], v[192:195], v[98:101]
	v_mfma_f32_16x16x32_bf16 v[86:89], v[168:171], v[200:203], v[86:89]
	v_mfma_f32_16x16x32_bf16 v[82:85], v[176:179], v[200:203], v[82:85]
	v_mfma_f32_16x16x32_bf16 v[70:73], v[168:171], v[208:211], v[70:73]
	v_mfma_f32_16x16x32_bf16 v[66:69], v[176:179], v[208:211], v[66:69]
	v_mfma_f32_16x16x32_bf16 v[118:121], v[172:175], v[188:191], v[118:121]
	v_mfma_f32_16x16x32_bf16 v[114:117], v[180:183], v[188:191], v[114:117]
	v_mfma_f32_16x16x32_bf16 v[102:105], v[172:175], v[196:199], v[102:105]
	v_mfma_f32_16x16x32_bf16 v[98:101], v[180:183], v[196:199], v[98:101]
	v_mfma_f32_16x16x32_bf16 v[86:89], v[172:175], v[204:207], v[86:89]
	v_mfma_f32_16x16x32_bf16 v[82:85], v[180:183], v[204:207], v[82:85]
	v_mfma_f32_16x16x32_bf16 v[70:73], v[172:175], v[212:215], v[70:73]
	v_mfma_f32_16x16x32_bf16 v[66:69], v[180:183], v[212:215], v[66:69]
	s_setprio 0
	s_barrier
	s_add_i32 s26, s70, s33
	v_lshl_add_u64 v[216:217], v[216:217], 0, s[8:9]
	s_mov_b32 m0, s26
	ds_read_b128 v[184:187], v154 offset:49152
	ds_read_b128 v[188:191], v154 offset:50176
	ds_read_b128 v[192:195], v154 offset:51200
	ds_read_b128 v[196:199], v154 offset:52224
	ds_read_b128 v[200:203], v154 offset:53248
	ds_read_b128 v[204:207], v154 offset:54272
	ds_read_b128 v[208:211], v154 offset:55296
	ds_read_b128 v[212:215], v154 offset:56320
	global_load_lds_dwordx4 v[216:217], off
	s_add_i32 m0, s26, 0x2000
	s_add_u32 s24, s24, 0x80080
	v_lshl_add_u64 v[216:217], v[218:219], 0, s[8:9]
	s_addc_u32 s25, s25, 0
	s_add_i32 s26, s71, s33
	global_load_lds_dwordx4 v[216:217], off
	v_lshl_add_u64 v[216:217], s[24:25], 0, v[134:135]
	s_mov_b32 m0, s26
	s_nop 0
	global_load_lds_dwordx4 v[216:217], off
	v_lshl_add_u64 v[216:217], s[24:25], 0, v[130:131]
	s_add_i32 m0, s26, 0x2000
	s_nop 0
	global_load_lds_dwordx4 v[216:217], off
	v_lshl_add_u64 v[216:217], v[220:221], 0, s[8:9]
	s_mov_b32 m0, s44
	s_nop 0
	global_load_lds_dwordx4 v[216:217], off
	v_lshl_add_u64 v[216:217], v[222:223], 0, s[8:9]
	s_mov_b32 m0, s45
	s_nop 0
	global_load_lds_dwordx4 v[216:217], off
	s_add_u32 s98, s98, 0x80
	s_addc_u32 s99, s99, 0
	s_mov_b32 m0, 0x21700
	s_nop 0
	global_load_lds_dword v252, s[98:99]
	s_waitcnt vmcnt(10)
	s_waitcnt lgkmcnt(0)
	s_barrier
	s_setprio 1
	s_waitcnt lgkmcnt(0)
	v_mfma_f32_16x16x32_bf16 v[62:65], v[146:149], v[184:187], v[62:65]
	v_mfma_f32_16x16x32_bf16 v[58:61], v[160:163], v[184:187], v[58:61]
	v_mfma_f32_16x16x32_bf16 v[46:49], v[146:149], v[192:195], v[46:49]
	v_mfma_f32_16x16x32_bf16 v[42:45], v[160:163], v[192:195], v[42:45]
	v_mfma_f32_16x16x32_bf16 v[30:33], v[146:149], v[200:203], v[30:33]
	v_mfma_f32_16x16x32_bf16 v[26:29], v[160:163], v[200:203], v[26:29]
	v_mfma_f32_16x16x32_bf16 v[14:17], v[146:149], v[208:211], v[14:17]
	v_mfma_f32_16x16x32_bf16 v[10:13], v[160:163], v[208:211], v[10:13]
	v_mfma_f32_16x16x32_bf16 v[62:65], v[156:159], v[188:191], v[62:65]
	v_mfma_f32_16x16x32_bf16 v[58:61], v[164:167], v[188:191], v[58:61]
	v_mfma_f32_16x16x32_bf16 v[46:49], v[156:159], v[196:199], v[46:49]
	v_mfma_f32_16x16x32_bf16 v[42:45], v[164:167], v[196:199], v[42:45]
	v_mfma_f32_16x16x32_bf16 v[30:33], v[156:159], v[204:207], v[30:33]
	v_mfma_f32_16x16x32_bf16 v[26:29], v[164:167], v[204:207], v[26:29]
	v_mfma_f32_16x16x32_bf16 v[14:17], v[156:159], v[212:215], v[14:17]
	v_mfma_f32_16x16x32_bf16 v[10:13], v[164:167], v[212:215], v[10:13]
	s_setprio 0
	s_setprio 1
	v_mfma_f32_16x16x32_bf16 v[54:57], v[168:171], v[184:187], v[54:57]
	v_mfma_f32_16x16x32_bf16 v[50:53], v[176:179], v[184:187], v[50:53]
	v_mfma_f32_16x16x32_bf16 v[38:41], v[168:171], v[192:195], v[38:41]
	v_mfma_f32_16x16x32_bf16 v[34:37], v[176:179], v[192:195], v[34:37]
	v_mfma_f32_16x16x32_bf16 v[22:25], v[168:171], v[200:203], v[22:25]
	v_mfma_f32_16x16x32_bf16 v[18:21], v[176:179], v[200:203], v[18:21]
	v_mfma_f32_16x16x32_bf16 v[6:9], v[168:171], v[208:211], v[6:9]
	v_mfma_f32_16x16x32_bf16 v[2:5], v[176:179], v[208:211], v[2:5]
	v_mfma_f32_16x16x32_bf16 v[54:57], v[172:175], v[188:191], v[54:57]
	v_mfma_f32_16x16x32_bf16 v[50:53], v[180:183], v[188:191], v[50:53]
	v_mfma_f32_16x16x32_bf16 v[38:41], v[172:175], v[196:199], v[38:41]
	v_mfma_f32_16x16x32_bf16 v[34:37], v[180:183], v[196:199], v[34:37]
	v_mfma_f32_16x16x32_bf16 v[22:25], v[172:175], v[204:207], v[22:25]
	v_mfma_f32_16x16x32_bf16 v[18:21], v[180:183], v[204:207], v[18:21]
	v_mfma_f32_16x16x32_bf16 v[6:9], v[172:175], v[212:215], v[6:9]
	v_mfma_f32_16x16x32_bf16 v[2:5], v[180:183], v[212:215], v[2:5]
	s_setprio 0
	s_barrier
	s_add_i32 s69, s69, 2
	s_add_u32 s22, s22, 0x100
	s_addc_u32 s23, s23, 0
	s_add_u32 s67, s67, 0x100
	s_addc_u32 s68, s68, 0
	s_cmp_gt_u32 s69, 29
	s_cbranch_scc0 .LBB0_574
	s_and_b64 vcc, exec, s[10:11]
	s_cbranch_vccz .LBB0_577
	s_barrier
